# attention tile-0 K fragment reads batched (one LDS wait chain instead of eight round trips), on the non-temporal stack
# baseline (speedup 1.0000x reference)
.LBB0_1063:
	s_mul_hi_i32 s26, s13, 0x55555556
	s_lshr_b32 s27, s26, 31
	s_add_i32 s28, s26, s27
	s_mul_i32 s27, s58, 0x1100000
	s_mul_hi_i32 s26, s58, 0x1100000
	s_add_u32 s29, s66, s27
	s_addc_u32 s34, s67, s26
	s_and_b64 s[26:27], exec, s[24:25]
	s_movk_i32 s26, 0xb00
	s_cselect_b32 s26, 0x600, s26
	s_add_u32 s29, s29, s26
	s_addc_u32 s34, s34, 0
	s_lshl_b32 s26, s13, 6
	s_ashr_i32 s27, s26, 31
	s_lshl_b64 s[26:27], s[26:27], 1
	s_add_u32 s40, s29, s26
	s_addc_u32 s41, s34, s27
	s_lshl_b32 s12, s12, 4
	s_lshl_b32 s13, s58, 1
	s_add_i32 s12, s12, s28
	s_add_i32 s12, s12, s13
	s_mul_hi_i32 s13, s12, 0x88000
	s_mul_i32 s12, s12, 0x88000
	s_waitcnt lgkmcnt(0)
	s_add_u32 s8, s8, s12
	s_addc_u32 s9, s9, s13
	s_add_u32 s10, s10, s12
	s_waitcnt vmcnt(11)
	v_mbcnt_lo_u32_b32 v36, -1, 0
	v_mbcnt_hi_u32_b32 v36, -1, v36
	s_getreg_b32 s12, hwreg(HW_REG_HW_ID, 0, 6)
	s_addc_u32 s11, s11, s13
	s_lshl_b32 s12, s12, 2
	s_and_b32 s12, s12, 0xfc
	s_or_b32 s12, s12, 0x27100
	v_mov_b32_e32 v0, s12
	ds_read_b32 v0, v0
	s_and_b64 vcc, s[6:7], s[24:25]
	v_and_b32_e32 v211, 63, v36
	v_and_b32_e32 v231, 31, v36
	v_bfe_u32 v232, v36, 5, 1
	s_waitcnt lgkmcnt(0)
	v_readfirstlane_b32 s12, v0
	v_lshlrev_b32_e32 v0, 7, v211
	v_lshl_add_u64 v[2:3], s[8:9], 0, v[0:1]
	v_lshl_or_b32 v4, s12, 6, v36
	v_bfe_u32 v0, v36, 2, 4
	v_readfirstlane_b32 s13, v4
	s_ashr_i32 s89, s13, 6
	s_lshl_b32 s37, s89, 5
	s_add_i32 s28, s37, s36
	s_ashr_i32 s29, s28, 31
	s_lshl_b64 s[34:35], s[28:29], 12
	s_add_u32 s34, s40, s34
	s_addc_u32 s35, s41, s35
	s_lshl_b32 s8, s89, 3
	s_ashr_i32 s9, s8, 31
	v_lshl_add_u64 v[2:3], s[8:9], 1, v[2:3]
	s_mov_b64 s[8:9], 0x5a800000
	v_lshl_add_u64 v[206:207], v[2:3], 0, s[8:9]
	s_lshl_b32 s8, s89, 4
	v_and_or_b32 v0, s8, 48, v0
	s_ashr_i32 s8, s13, 3
	v_lshlrev_b32_e32 v0, 7, v0
	s_andn2_b32 s8, s8, 31
	v_lshlrev_b32_e32 v230, 3, v4
	v_lshl_add_u64 v[2:3], s[10:11], 0, v[0:1]
	s_ashr_i32 s9, s8, 31
	v_and_b32_e32 v234, 24, v230
	v_lshl_add_u64 v[2:3], s[8:9], 1, v[2:3]
	v_lshlrev_b32_e32 v0, 1, v234
	s_lshl_b32 s12, s89, 10
	v_lshl_add_u64 v[2:3], v[2:3], 0, v[0:1]
	s_mov_b64 s[8:9], 0x5cc00000
	s_cmp_lg_u32 0, -1
	v_lshl_add_u64 v[208:209], v[2:3], 0, s[8:9]
	s_cselect_b32 s8, 0, 0
	s_lshl_b32 s70, s69, 7
	s_add_i32 s45, s12, s8
	v_lshl_add_u64 v[34:35], v[206:207], 0, s[70:71]
	s_mov_b32 s8, m0
	s_mov_b32 m0, s45
	s_nop 0
	global_load_lds_dwordx4 v[34:35], off
	s_mov_b32 m0, s8
	s_add_i32 s44, s45, 0x6000
	v_lshl_add_u64 v[2:3], v[208:209], 0, s[70:71]
	s_mov_b32 s8, m0
	s_mov_b32 m0, s44
	s_nop 0
	global_load_lds_dwordx4 v[2:3], off
	s_mov_b32 m0, s8
	s_bitset1_b32 s70, 13
	v_lshlrev_b32_e32 v0, 12, v231
	v_lshl_add_u64 v[2:3], v[206:207], 0, s[70:71]
	s_add_i32 s8, s45, 0x2000
	s_mov_b32 s9, m0
	s_mov_b32 m0, s8
	s_nop 0
	global_load_lds_dwordx4 v[2:3], off
	s_mov_b32 m0, s9
	v_lshl_or_b32 v0, v232, 4, v0
	global_load_dwordx4 v[152:155], v0, s[34:35] nt
	global_load_dwordx4 v[144:147], v0, s[34:35] offset:32 nt
	global_load_dwordx4 v[132:135], v0, s[34:35] offset:64 nt
	global_load_dwordx4 v[128:131], v0, s[34:35] offset:96 nt
	v_mov_b32_e32 v2, v1
	v_mov_b32_e32 v3, v1
	v_mov_b32_e32 v4, v1
	v_mov_b32_e32 v5, v1
	v_mov_b32_e32 v6, v1
	v_mov_b32_e32 v7, v1
	v_mov_b32_e32 v8, v1
	v_mov_b32_e32 v9, v1
	v_mov_b32_e32 v10, v1
	v_mov_b32_e32 v11, v1
	v_mov_b32_e32 v12, v1
	v_mov_b32_e32 v13, v1
	v_mov_b32_e32 v14, v1
	v_mov_b32_e32 v15, v1
	v_lshlrev_b32_e32 v0, 10, v232
	v_lshlrev_b32_e32 v16, 4, v231
	v_add3_u32 v240, 0, v0, v16
	v_mov_b32_e32 v0, v1
	v_mov_b64_e32 v[16:17], v[14:15]
	v_mov_b64_e32 v[14:15], v[12:13]
	v_mov_b64_e32 v[12:13], v[10:11]
	v_mov_b64_e32 v[10:11], v[8:9]
	v_mov_b64_e32 v[8:9], v[6:7]
	v_mov_b64_e32 v[6:7], v[4:5]
	v_mov_b64_e32 v[4:5], v[2:3]
	v_mov_b64_e32 v[2:3], v[0:1]
	s_mov_b64 s[8:9], 0x4000
	v_lshl_add_u64 v[18:19], v[34:35], 0, s[8:9]
	s_add_i32 s8, s45, 0x4000
	s_mov_b32 s9, m0
	s_mov_b32 m0, s8
	s_nop 0
	global_load_lds_dwordx4 v[18:19], off
	s_mov_b32 m0, s9
	s_waitcnt vmcnt(3) lgkmcnt(0)
	s_barrier
	s_waitcnt vmcnt(14)
	ds_read_b128 v[160:163], v240
	ds_read_b128 v[164:167], v240 offset:512
	ds_read_b128 v[168:171], v240 offset:2048
	ds_read_b128 v[172:175], v240 offset:2560
	ds_read_b128 v[176:179], v240 offset:4096
	ds_read_b128 v[180:183], v240 offset:4608
	ds_read_b128 v[184:187], v240 offset:6144
	ds_read_b128 v[188:191], v240 offset:6656
	v_cndmask_b32_e32 v0, 0, v210, vcc
	v_cmp_nlt_f32_e64 s[8:9], 0, v0
	s_and_b64 vcc, exec, s[8:9]
	s_waitcnt vmcnt(3) lgkmcnt(7)
	v_mfma_f32_32x32x16_bf16 v[18:33], v[160:163], v[152:155], v[2:17]
	s_waitcnt lgkmcnt(6)
	v_mfma_f32_32x32x16_bf16 v[2:17], v[164:167], v[152:155], v[2:17]
	s_waitcnt vmcnt(2) lgkmcnt(5)
	v_mfma_f32_32x32x16_bf16 v[18:33], v[168:171], v[144:147], v[18:33]
	s_waitcnt lgkmcnt(4)
	v_mfma_f32_32x32x16_bf16 v[2:17], v[172:175], v[144:147], v[2:17]
	s_waitcnt vmcnt(1) lgkmcnt(3)
	v_mfma_f32_32x32x16_bf16 v[18:33], v[176:179], v[132:135], v[18:33]
	s_waitcnt lgkmcnt(2)
	v_mfma_f32_32x32x16_bf16 v[2:17], v[180:183], v[132:135], v[2:17]
	s_waitcnt vmcnt(0) lgkmcnt(1)
	v_mfma_f32_32x32x16_bf16 v[18:33], v[184:187], v[128:131], v[18:33]
	s_waitcnt lgkmcnt(0)
	v_mfma_f32_32x32x16_bf16 v[2:17], v[188:191], v[128:131], v[2:17]
	s_nop 15
	s_nop 7
	s_cbranch_vccz .LBB0_1065
	v_max3_f32 v37, v18, v19, v2
	v_max3_f32 v38, v20, v21, v3
	s_nop 0
	v_max3_f32 v37, v37, v4, v5
	v_max3_f32 v38, v38, v24, v25
	s_nop 0
	v_max3_f32 v37, v37, v22, v23
	v_max3_f32 v38, v38, v8, v9
	s_nop 0
	v_max3_f32 v37, v37, v6, v7
	v_max3_f32 v38, v38, v28, v29
	s_nop 0
	v_max3_f32 v37, v37, v26, v27
	v_max3_f32 v38, v38, v12, v13
	s_nop 0
	v_max3_f32 v37, v37, v10, v11
	v_max3_f32 v38, v38, v32, v33
	s_nop 0
	v_max3_f32 v37, v37, v30, v31
	v_max3_f32 v38, v38, v16, v17
	s_nop 0
	v_max3_f32 v37, v37, v14, v15
	s_nop 0
	v_max_f32_e32 v37, v37, v38
	s_nop 0
	v_mov_b32_e32 v38, v37
	s_nop 1
	v_permlane32_swap_b32_e32 v37, v38
	v_max_f32_e32 v37, v37, v38
	s_cbranch_execz .LBB0_1066
	s_branch .LBB0_1067
